# router partial logits + row sums of squares computed in the out-projection epilogue (bf16 MFMA on hi+lo weights, fixed-point LDS combine), router phase reads 12 MB of partials instead of x1 and weight
# speedup vs baseline: 1.0192x; 1.0146x over previous
; __device__ __forceinline__ unsigned cvt_pk_bf16(float lo, float hi) { unsigned r; asm volatile("v_cvt_pk_bf16_f32 %0, %1, %2" : "=v"(r) : "v"(lo), "v"(hi)); return r; }
; __device__ __forceinline__ unsigned pk4_fp8(float a, float b, float c, float d) { int p = 0; p = __builtin_amdgcn_cvt_pk_fp8_f32(a, b, p, false); p = __builtin_amdgcn_cvt_pk_fp8_f32(c, d, p, true); return (unsigned)p; }
;     __device__ __forceinline__ void operator()(AccRef acc, const Unit& u, int wr, int wc, int fr, int fq) const {
;         const int row0 = u.pm * BM + wr * 64 + fr, col0 = u.pn * BM + wc * 32 + 8 * fq;
;         f32x4 gv[2][2];
; #pragma unroll
;         for (int bj = 0; bj < 2; ++bj)
; #pragma unroll
;             for (int n = 0; n < 2; ++n) gv[bj][n] = *(const f32x4*)(g2 + col0 + bj * HALF + 4 * n);
; #pragma unroll
;         for (int ai = 0; ai < 2; ++ai)
; #pragma unroll
;             for (int m = 0; m < 4; ++m) { const size_t ro = (size_t)(row0 + ai * HALF + m * 16) * DM + col0;
;                 f32x4 xv[2][2];
; #pragma unroll
;                 for (int bj = 0; bj < 2; ++bj)
; #pragma unroll
;                     for (int n = 0; n < 2; ++n) xv[bj][n] = __builtin_nontemporal_load((const f32x4*)(X + ro + bj * HALF + 4 * n));
; #pragma unroll
;                 for (int bj = 0; bj < 2; ++bj) { const f32x4 a = xv[bj][0] + acc[ai][bj][m][0], b = xv[bj][1] + acc[ai][bj][m][1];
;                     { v4u xo; xo.x = cvt_pk_bf16(a[0], a[1]); xo.y = cvt_pk_bf16(a[2], a[3]); xo.z = cvt_pk_bf16(b[0], b[1]); xo.w = cvt_pk_bf16(b[2], b[3]); *(v4u*)(O + ro + bj * HALF) = xo; }
;                     const f32x4 ha = a * gv[bj][0], hb = b * gv[bj][1];
;                     v2u w; w.x = pk4_fp8(ha[0], ha[1], ha[2], ha[3]); w.y = pk4_fp8(hb[0], hb[1], hb[2], hb[3]);
;                     *(v2u*)((unsigned char*)HN + ro + bj * HALF) = w; } }
.LBB0_489:
	v_lshlrev_b32_e32 v241, 1, v254
	v_and_b32_e32 v252, 0x7ff, v254
	v_mbcnt_lo_u32_b32 v243, -1, 0
	v_mbcnt_hi_u32_b32 v243, -1, v243
	v_and_b32_e32 v243, 15, v243
	v_lshl_add_u32 v243, v243, 11, v252
	v_lshlrev_b32_e32 v243, 1, v243
	v_lshlrev_b32_e32 v252, 2, v252
	global_load_dwordx4 v[108:111], v252, s[10:11]
	global_load_dwordx4 v[104:107], v252, s[10:11] offset:16
	global_load_dwordx4 v[100:103], v252, s[10:11] offset:512
	global_load_dwordx4 v[96:99], v252, s[10:11] offset:528
	s_add_u32 s12, s36, 0x40000
	s_addc_u32 s13, s37, 0
	global_load_dwordx4 v[164:167], v240, s[12:13] nt
	global_load_dwordx4 v[168:171], v240, s[12:13] offset:16 nt
	global_load_dwordx4 v[172:175], v240, s[12:13] offset:512 nt
	global_load_dwordx4 v[176:179], v240, s[12:13] offset:528 nt
	s_add_u32 s12, s36, 0x60000
	s_addc_u32 s13, s37, 0
	global_load_dwordx4 v[180:183], v240, s[12:13] nt
	global_load_dwordx4 v[184:187], v240, s[12:13] offset:16 nt
	global_load_dwordx4 v[188:191], v240, s[12:13] offset:512 nt
	global_load_dwordx4 v[192:195], v240, s[12:13] offset:528 nt
	s_add_u32 s12, s36, 0x100000
	s_addc_u32 s13, s37, 0
	global_load_dwordx4 v[196:199], v240, s[12:13] nt
	global_load_dwordx4 v[200:203], v240, s[12:13] offset:16 nt
	global_load_dwordx4 v[204:207], v240, s[12:13] offset:512 nt
	global_load_dwordx4 v[148:151], v240, s[12:13] offset:528 nt
	s_nop 1
	s_waitcnt vmcnt(12)
	v_pk_add_f32 v[140:141], v[140:141], v[208:209]
	v_pk_add_f32 v[142:143], v[142:143], v[210:211]
	v_pk_add_f32 v[136:137], v[136:137], v[212:213]
	v_pk_add_f32 v[138:139], v[138:139], v[214:215]
	v_pk_add_f32 v[132:133], v[132:133], v[216:217]
	v_pk_add_f32 v[134:135], v[134:135], v[218:219]
	v_pk_add_f32 v[128:129], v[128:129], v[220:221]
	v_pk_add_f32 v[130:131], v[130:131], v[222:223]
	s_add_u32 s16, s38, 0x0
	s_addc_u32 s17, s39, 0
	s_add_u32 s20, s60, 0x0
	s_addc_u32 s21, s61, 0
	v_pk_mul_f32 v[208:209], v[108:109], v[140:141]
	v_pk_mul_f32 v[210:211], v[110:111], v[142:143]
	v_pk_mul_f32 v[212:213], v[104:105], v[136:137]
	v_pk_mul_f32 v[214:215], v[106:107], v[138:139]
	v_pk_mul_f32 v[216:217], v[100:101], v[132:133]
	v_pk_mul_f32 v[218:219], v[102:103], v[134:135]
	v_pk_mul_f32 v[220:221], v[96:97], v[128:129]
	v_pk_mul_f32 v[222:223], v[98:99], v[130:131]
	s_nop 0
	v_cvt_pk_bf16_f32 v140, v140, v141
	v_cvt_pk_bf16_f32 v141, v142, v143
	v_cvt_pk_bf16_f32 v142, v136, v137
	v_cvt_pk_bf16_f32 v143, v138, v139
	v_cvt_pk_bf16_f32 v132, v132, v133
	v_cvt_pk_bf16_f32 v133, v134, v135
	v_cvt_pk_bf16_f32 v134, v128, v129
	v_cvt_pk_bf16_f32 v135, v130, v131
	global_store_dwordx4 v241, v[140:143], s[16:17]
	global_store_dwordx4 v241, v[132:135], s[16:17] offset:256
	v_cvt_pk_fp8_f32 v252, v208, v209
	v_cvt_pk_fp8_f32 v253, v212, v213
	v_cvt_pk_fp8_f32 v242, v216, v217
	v_cvt_pk_fp8_f32 v243, v220, v221
	v_cvt_pk_fp8_f32 v252, v210, v211 op_sel:[0,0,1]
	v_cvt_pk_fp8_f32 v253, v214, v215 op_sel:[0,0,1]
	v_cvt_pk_fp8_f32 v242, v218, v219 op_sel:[0,0,1]
	v_cvt_pk_fp8_f32 v243, v222, v223 op_sel:[0,0,1]
	s_nop 0
	global_store_dwordx2 v254, v[252:253], s[20:21]
	global_store_dwordx2 v254, v[242:243], s[20:21] offset:128
	s_nop 1
	s_add_u32 s12, s36, 0x120000
	s_addc_u32 s13, s37, 0
	global_load_dwordx4 v[208:211], v240, s[12:13] nt
	global_load_dwordx4 v[212:215], v240, s[12:13] offset:16 nt
	global_load_dwordx4 v[216:219], v240, s[12:13] offset:512 nt
	global_load_dwordx4 v[220:223], v240, s[12:13] offset:528 nt
	v_pk_add_f32 v[124:125], v[124:125], v[224:225]
	v_pk_add_f32 v[126:127], v[126:127], v[226:227]
	v_pk_add_f32 v[120:121], v[120:121], v[228:229]
	v_pk_add_f32 v[122:123], v[122:123], v[230:231]
	v_pk_add_f32 v[116:117], v[116:117], v[232:233]
	v_pk_add_f32 v[118:119], v[118:119], v[234:235]
	v_pk_add_f32 v[112:113], v[112:113], v[236:237]
	v_pk_add_f32 v[114:115], v[114:115], v[238:239]
	s_add_u32 s16, s38, 0x10000
	s_addc_u32 s17, s39, 0
	s_add_u32 s20, s60, 0x8000
	s_addc_u32 s21, s61, 0
	v_pk_mul_f32 v[224:225], v[108:109], v[124:125]
	v_pk_mul_f32 v[226:227], v[110:111], v[126:127]
	v_pk_mul_f32 v[228:229], v[104:105], v[120:121]
	v_pk_mul_f32 v[230:231], v[106:107], v[122:123]
	v_pk_mul_f32 v[232:233], v[100:101], v[116:117]
	v_pk_mul_f32 v[234:235], v[102:103], v[118:119]
	v_pk_mul_f32 v[236:237], v[96:97], v[112:113]
	v_pk_mul_f32 v[238:239], v[98:99], v[114:115]
	s_nop 0
	v_cvt_pk_bf16_f32 v124, v124, v125
	v_cvt_pk_bf16_f32 v125, v126, v127
	v_cvt_pk_bf16_f32 v126, v120, v121
	v_cvt_pk_bf16_f32 v127, v122, v123
	v_cvt_pk_bf16_f32 v116, v116, v117
	v_cvt_pk_bf16_f32 v117, v118, v119
	v_cvt_pk_bf16_f32 v118, v112, v113
	v_cvt_pk_bf16_f32 v119, v114, v115
	global_store_dwordx4 v241, v[124:127], s[16:17]
	global_store_dwordx4 v241, v[116:119], s[16:17] offset:256
	v_cvt_pk_fp8_f32 v252, v224, v225
	v_cvt_pk_fp8_f32 v253, v228, v229
	v_cvt_pk_fp8_f32 v242, v232, v233
	v_cvt_pk_fp8_f32 v243, v236, v237
	v_cvt_pk_fp8_f32 v252, v226, v227 op_sel:[0,0,1]
	v_cvt_pk_fp8_f32 v253, v230, v231 op_sel:[0,0,1]
	v_cvt_pk_fp8_f32 v242, v234, v235 op_sel:[0,0,1]
	v_cvt_pk_fp8_f32 v243, v238, v239 op_sel:[0,0,1]
	s_nop 0
	global_store_dwordx2 v254, v[252:253], s[20:21]
	global_store_dwordx2 v254, v[242:243], s[20:21] offset:128
	s_nop 1
	s_add_u32 s12, s36, 0x140000
	s_addc_u32 s13, s37, 0
	global_load_dwordx4 v[224:227], v240, s[12:13] nt
	global_load_dwordx4 v[228:231], v240, s[12:13] offset:16 nt
	global_load_dwordx4 v[232:235], v240, s[12:13] offset:512 nt
	global_load_dwordx4 v[236:239], v240, s[12:13] offset:528 nt
	s_waitcnt vmcnt(24)
; __device__ __forceinline__ unsigned cvt_pk_bf16(float lo, float hi) { unsigned r; asm volatile("v_cvt_pk_bf16_f32 %0, %1, %2" : "=v"(r) : "v"(lo), "v"(hi)); return r; }
; __device__ __forceinline__ unsigned pk4_fp8(float a, float b, float c, float d) { int p = 0; p = __builtin_amdgcn_cvt_pk_fp8_f32(a, b, p, false); p = __builtin_amdgcn_cvt_pk_fp8_f32(c, d, p, true); return (unsigned)p; }
;     __device__ __forceinline__ void operator()(AccRef acc, const Unit& u, int wr, int wc, int fr, int fq) const {
;     ...
;         for (int ai = 0; ai < 2; ++ai)
; #pragma unroll
;             for (int m = 0; m < 4; ++m) { const size_t ro = (size_t)(row0 + ai * HALF + m * 16) * DM + col0;
;                 f32x4 xv[2][2];
; #pragma unroll
;                 for (int bj = 0; bj < 2; ++bj)
; #pragma unroll
;                     for (int n = 0; n < 2; ++n) xv[bj][n] = __builtin_nontemporal_load((const f32x4*)(X + ro + bj * HALF + 4 * n));
; #pragma unroll
;                 for (int bj = 0; bj < 2; ++bj) { const f32x4 a = xv[bj][0] + acc[ai][bj][m][0], b = xv[bj][1] + acc[ai][bj][m][1];
;                     { v4u xo; xo.x = cvt_pk_bf16(a[0], a[1]); xo.y = cvt_pk_bf16(a[2], a[3]); xo.z = cvt_pk_bf16(b[0], b[1]); xo.w = cvt_pk_bf16(b[2], b[3]); *(v4u*)(O + ro + bj * HALF) = xo; }
;                     const f32x4 ha = a * gv[bj][0], hb = b * gv[bj][1];
;                     v2u w; w.x = pk4_fp8(ha[0], ha[1], ha[2], ha[3]); w.y = pk4_fp8(hb[0], hb[1], hb[2], hb[3]);
;                     *(v2u*)((unsigned char*)HN + ro + bj * HALF) = w; } }
; __global__ void __launch_bounds__(512, 2) hymba_fwd(Args args) {
;     ...
;                     for (int s4 = 0; s4 < 4; ++s4) { const int ko = 32 * (4 * hf + s4);
; #pragma unroll
;                         for (int x = 0; x < 2; ++x) xa[x][s4] = *(const v4u*)(xp + (size_t)(16 * x) * DM + ko);
; #pragma unroll
;                         for (int nt = 0; nt < 3; ++nt) { bh[s4][nt] = *(const bf16x8*)(hp + (size_t)(16 * nt) * DM + ko); bl[s4][nt] = *(const bf16x8*)(lp + (size_t)(16 * nt) * DM + ko); } }
	v_pk_add_f32 v[92:93], v[92:93], v[164:165]
	v_pk_add_f32 v[94:95], v[94:95], v[166:167]
	v_pk_add_f32 v[88:89], v[88:89], v[168:169]
	v_pk_add_f32 v[90:91], v[90:91], v[170:171]
	v_pk_add_f32 v[84:85], v[84:85], v[172:173]
	v_pk_add_f32 v[86:87], v[86:87], v[174:175]
	v_pk_add_f32 v[80:81], v[80:81], v[176:177]
	v_pk_add_f32 v[82:83], v[82:83], v[178:179]
	s_add_u32 s16, s38, 0x20000
	s_addc_u32 s17, s39, 0
	s_add_u32 s20, s60, 0x10000
	s_addc_u32 s21, s61, 0
	v_pk_mul_f32 v[164:165], v[108:109], v[92:93]
	v_pk_mul_f32 v[166:167], v[110:111], v[94:95]
	v_pk_mul_f32 v[168:169], v[104:105], v[88:89]
	v_pk_mul_f32 v[170:171], v[106:107], v[90:91]
	v_pk_mul_f32 v[172:173], v[100:101], v[84:85]
	v_pk_mul_f32 v[174:175], v[102:103], v[86:87]
	v_pk_mul_f32 v[176:177], v[96:97], v[80:81]
	v_pk_mul_f32 v[178:179], v[98:99], v[82:83]
	s_nop 0
	v_cvt_pk_bf16_f32 v92, v92, v93
	v_cvt_pk_bf16_f32 v93, v94, v95
	v_cvt_pk_bf16_f32 v94, v88, v89
	v_cvt_pk_bf16_f32 v95, v90, v91
	v_cvt_pk_bf16_f32 v84, v84, v85
	v_cvt_pk_bf16_f32 v85, v86, v87
	v_cvt_pk_bf16_f32 v86, v80, v81
	v_cvt_pk_bf16_f32 v87, v82, v83
	global_store_dwordx4 v241, v[92:95], s[16:17]
	global_store_dwordx4 v241, v[84:87], s[16:17] offset:256
	v_cvt_pk_fp8_f32 v252, v164, v165
	v_cvt_pk_fp8_f32 v253, v168, v169
	v_cvt_pk_fp8_f32 v242, v172, v173
	v_cvt_pk_fp8_f32 v243, v176, v177
	v_cvt_pk_fp8_f32 v252, v166, v167 op_sel:[0,0,1]
	v_cvt_pk_fp8_f32 v253, v170, v171 op_sel:[0,0,1]
	v_cvt_pk_fp8_f32 v242, v174, v175 op_sel:[0,0,1]
	v_cvt_pk_fp8_f32 v243, v178, v179 op_sel:[0,0,1]
	s_nop 0
	global_store_dwordx2 v254, v[252:253], s[20:21]
	global_store_dwordx2 v254, v[242:243], s[20:21] offset:128
	s_nop 1
	s_add_u32 s12, s36, 0x160000
	s_addc_u32 s13, s37, 0
	global_load_dwordx4 v[164:167], v240, s[12:13] nt
	global_load_dwordx4 v[168:171], v240, s[12:13] offset:16 nt
	global_load_dwordx4 v[172:175], v240, s[12:13] offset:512 nt
	global_load_dwordx4 v[176:179], v240, s[12:13] offset:528 nt
	s_waitcnt vmcnt(28)
	v_pk_add_f32 v[76:77], v[76:77], v[180:181]
	v_pk_add_f32 v[78:79], v[78:79], v[182:183]
	v_pk_add_f32 v[72:73], v[72:73], v[184:185]
	v_pk_add_f32 v[74:75], v[74:75], v[186:187]
	v_pk_add_f32 v[68:69], v[68:69], v[188:189]
	v_pk_add_f32 v[70:71], v[70:71], v[190:191]
	v_pk_add_f32 v[64:65], v[64:65], v[192:193]
	v_pk_add_f32 v[66:67], v[66:67], v[194:195]
	s_add_u32 s16, s38, 0x30000
	s_addc_u32 s17, s39, 0
	s_add_u32 s20, s60, 0x18000
	s_addc_u32 s21, s61, 0
	v_pk_mul_f32 v[180:181], v[108:109], v[76:77]
	v_pk_mul_f32 v[182:183], v[110:111], v[78:79]
	v_pk_mul_f32 v[184:185], v[104:105], v[72:73]
	v_pk_mul_f32 v[186:187], v[106:107], v[74:75]
	v_pk_mul_f32 v[188:189], v[100:101], v[68:69]
	v_pk_mul_f32 v[190:191], v[102:103], v[70:71]
	v_pk_mul_f32 v[192:193], v[96:97], v[64:65]
	v_pk_mul_f32 v[194:195], v[98:99], v[66:67]
	s_nop 0
	v_cvt_pk_bf16_f32 v76, v76, v77
	v_cvt_pk_bf16_f32 v77, v78, v79
	v_cvt_pk_bf16_f32 v78, v72, v73
	v_cvt_pk_bf16_f32 v79, v74, v75
	v_cvt_pk_bf16_f32 v68, v68, v69
	v_cvt_pk_bf16_f32 v69, v70, v71
	v_cvt_pk_bf16_f32 v70, v64, v65
	v_cvt_pk_bf16_f32 v71, v66, v67
	global_store_dwordx4 v241, v[76:79], s[16:17]
	global_store_dwordx4 v241, v[68:71], s[16:17] offset:256
	v_cvt_pk_fp8_f32 v252, v180, v181
	v_cvt_pk_fp8_f32 v253, v184, v185
	v_cvt_pk_fp8_f32 v242, v188, v189
	v_cvt_pk_fp8_f32 v243, v192, v193
	v_cvt_pk_fp8_f32 v252, v182, v183 op_sel:[0,0,1]
	v_cvt_pk_fp8_f32 v253, v186, v187 op_sel:[0,0,1]
	v_cvt_pk_fp8_f32 v242, v190, v191 op_sel:[0,0,1]
	v_cvt_pk_fp8_f32 v243, v194, v195 op_sel:[0,0,1]
	s_nop 0
	global_store_dwordx2 v254, v[252:253], s[20:21]
	global_store_dwordx2 v254, v[242:243], s[20:21] offset:128
	v_and_b32_e32 v244, 0x7ff, v254
	v_mbcnt_lo_u32_b32 v243, -1, 0
	v_mbcnt_hi_u32_b32 v243, -1, v243
	v_and_b32_e32 v243, 15, v243
	v_lshl_add_u32 v243, v243, 11, v244
	v_lshlrev_b32_e32 v243, 1, v243
	s_nop 1
	s_add_u32 s12, s26, 0x350000
	s_addc_u32 s13, s27, 0
	global_load_dwordx4 v[180:183], v243, s[12:13]
	s_add_u32 s12, s26, 0x320000
	s_addc_u32 s13, s27, 0
	global_load_dwordx4 v[184:187], v243, s[12:13]
	s_add_u32 s12, s26, 0x360000
	s_addc_u32 s13, s27, 0
	global_load_dwordx4 v[188:191], v243, s[12:13]
	s_add_u32 s12, s26, 0x330000
	s_addc_u32 s13, s27, 0
	global_load_dwordx4 v[192:195], v243, s[12:13]
	s_waitcnt vmcnt(32)
	v_pk_add_f32 v[60:61], v[60:61], v[196:197]
	v_pk_add_f32 v[62:63], v[62:63], v[198:199]
	v_pk_add_f32 v[56:57], v[56:57], v[200:201]
	v_pk_add_f32 v[58:59], v[58:59], v[202:203]
	v_pk_add_f32 v[52:53], v[52:53], v[204:205]
	v_pk_add_f32 v[54:55], v[54:55], v[206:207]
	v_pk_add_f32 v[48:49], v[48:49], v[148:149]
	v_pk_add_f32 v[50:51], v[50:51], v[150:151]
	s_add_u32 s16, s38, 0x80000
	s_addc_u32 s17, s39, 0
	s_add_u32 s20, s60, 0x40000
	s_addc_u32 s21, s61, 0
	v_pk_mul_f32 v[196:197], v[108:109], v[60:61]
	v_pk_mul_f32 v[198:199], v[110:111], v[62:63]
	v_pk_mul_f32 v[200:201], v[104:105], v[56:57]
	v_pk_mul_f32 v[202:203], v[106:107], v[58:59]
	v_pk_mul_f32 v[204:205], v[100:101], v[52:53]
	v_pk_mul_f32 v[206:207], v[102:103], v[54:55]
	v_pk_mul_f32 v[148:149], v[96:97], v[48:49]
	v_pk_mul_f32 v[150:151], v[98:99], v[50:51]
	s_nop 0
	v_cvt_pk_bf16_f32 v60, v60, v61
	v_cvt_pk_bf16_f32 v61, v62, v63
	v_cvt_pk_bf16_f32 v62, v56, v57
	v_cvt_pk_bf16_f32 v63, v58, v59
	v_cvt_pk_bf16_f32 v52, v52, v53
	v_cvt_pk_bf16_f32 v53, v54, v55
	v_cvt_pk_bf16_f32 v54, v48, v49
	v_cvt_pk_bf16_f32 v55, v50, v51
	global_store_dwordx4 v241, v[60:63], s[16:17]
	global_store_dwordx4 v241, v[52:55], s[16:17] offset:256
	v_cvt_pk_fp8_f32 v252, v196, v197
	v_cvt_pk_fp8_f32 v253, v200, v201
	v_cvt_pk_fp8_f32 v242, v204, v205
	v_cvt_pk_fp8_f32 v243, v148, v149
	v_cvt_pk_fp8_f32 v252, v198, v199 op_sel:[0,0,1]
	v_cvt_pk_fp8_f32 v253, v202, v203 op_sel:[0,0,1]
	v_cvt_pk_fp8_f32 v242, v206, v207 op_sel:[0,0,1]
	v_cvt_pk_fp8_f32 v243, v150, v151 op_sel:[0,0,1]
	s_nop 0
	global_store_dwordx2 v254, v[252:253], s[20:21]
	global_store_dwordx2 v254, v[242:243], s[20:21] offset:128
	v_and_b32_e32 v244, 0x7ff, v254
	v_mbcnt_lo_u32_b32 v243, -1, 0
	v_mbcnt_hi_u32_b32 v243, -1, v243
	v_and_b32_e32 v243, 15, v243
	v_lshl_add_u32 v243, v243, 11, v244
	v_lshlrev_b32_e32 v243, 1, v243
	s_nop 1
	s_add_u32 s12, s26, 0x370000
	s_addc_u32 s13, s27, 0
	global_load_dwordx4 v[196:199], v243, s[12:13]
	s_add_u32 s12, s26, 0x340000
	s_addc_u32 s13, s27, 0
	global_load_dwordx4 v[200:203], v243, s[12:13]
	s_add_u32 s12, s26, 0x350100
	s_addc_u32 s13, s27, 0
	global_load_dwordx4 v[204:207], v243, s[12:13]
	s_add_u32 s12, s26, 0x320100
	s_addc_u32 s13, s27, 0
	global_load_dwordx4 v[148:151], v243, s[12:13]
	s_waitcnt vmcnt(32)
; __device__ __forceinline__ unsigned cvt_pk_bf16(float lo, float hi) { unsigned r; asm volatile("v_cvt_pk_bf16_f32 %0, %1, %2" : "=v"(r) : "v"(lo), "v"(hi)); return r; }
; __device__ __forceinline__ unsigned pk4_fp8(float a, float b, float c, float d) { int p = 0; p = __builtin_amdgcn_cvt_pk_fp8_f32(a, b, p, false); p = __builtin_amdgcn_cvt_pk_fp8_f32(c, d, p, true); return (unsigned)p; }
;     __device__ __forceinline__ void operator()(AccRef acc, const Unit& u, int wr, int wc, int fr, int fq) const {
;     ...
;         for (int ai = 0; ai < 2; ++ai)
; #pragma unroll
;             for (int m = 0; m < 4; ++m) { const size_t ro = (size_t)(row0 + ai * HALF + m * 16) * DM + col0;
;                 f32x4 xv[2][2];
; #pragma unroll
;                 for (int bj = 0; bj < 2; ++bj)
; #pragma unroll
;                     for (int n = 0; n < 2; ++n) xv[bj][n] = __builtin_nontemporal_load((const f32x4*)(X + ro + bj * HALF + 4 * n));
; #pragma unroll
;                 for (int bj = 0; bj < 2; ++bj) { const f32x4 a = xv[bj][0] + acc[ai][bj][m][0], b = xv[bj][1] + acc[ai][bj][m][1];
;                     { v4u xo; xo.x = cvt_pk_bf16(a[0], a[1]); xo.y = cvt_pk_bf16(a[2], a[3]); xo.z = cvt_pk_bf16(b[0], b[1]); xo.w = cvt_pk_bf16(b[2], b[3]); *(v4u*)(O + ro + bj * HALF) = xo; }
;                     const f32x4 ha = a * gv[bj][0], hb = b * gv[bj][1];
;                     v2u w; w.x = pk4_fp8(ha[0], ha[1], ha[2], ha[3]); w.y = pk4_fp8(hb[0], hb[1], hb[2], hb[3]);
;                     *(v2u*)((unsigned char*)HN + ro + bj * HALF) = w; } }
; __global__ void __launch_bounds__(512, 2) hymba_fwd(Args args) {
;     ...
;                 for (int x = 0; x < 2; ++x) {
; #pragma unroll
;                     for (int nt = 0; nt < 3; ++nt)
; #pragma unroll
;                         for (int e = 0; e < 4; ++e) part[(wave * 32 + 16 * x + 4 * kg + e) * 48 + 16 * nt + li] = acc[x][nt][e];
;                     float s1 = ss[x]; s1 += __shfl_xor(s1, 16); s1 += __shfl_xor(s1, 32);
;                     if (kg == 0) ssp[wave * 32 + 16 * x + li] = s1; }
	v_pk_add_f32 v[44:45], v[44:45], v[208:209]
	v_pk_add_f32 v[46:47], v[46:47], v[210:211]
	v_pk_add_f32 v[40:41], v[40:41], v[212:213]
	v_pk_add_f32 v[42:43], v[42:43], v[214:215]
	v_pk_add_f32 v[36:37], v[36:37], v[216:217]
	v_pk_add_f32 v[38:39], v[38:39], v[218:219]
	v_pk_add_f32 v[32:33], v[32:33], v[220:221]
	v_pk_add_f32 v[34:35], v[34:35], v[222:223]
	s_add_u32 s16, s38, 0x90000
	s_addc_u32 s17, s39, 0
	s_add_u32 s20, s60, 0x48000
	s_addc_u32 s21, s61, 0
	v_pk_mul_f32 v[208:209], v[108:109], v[44:45]
	v_pk_mul_f32 v[210:211], v[110:111], v[46:47]
	v_pk_mul_f32 v[212:213], v[104:105], v[40:41]
	v_pk_mul_f32 v[214:215], v[106:107], v[42:43]
	v_pk_mul_f32 v[216:217], v[100:101], v[36:37]
	v_pk_mul_f32 v[218:219], v[102:103], v[38:39]
	v_pk_mul_f32 v[220:221], v[96:97], v[32:33]
	v_pk_mul_f32 v[222:223], v[98:99], v[34:35]
	s_nop 0
	v_cvt_pk_bf16_f32 v44, v44, v45
	v_cvt_pk_bf16_f32 v45, v46, v47
	v_cvt_pk_bf16_f32 v46, v40, v41
	v_cvt_pk_bf16_f32 v47, v42, v43
	v_cvt_pk_bf16_f32 v36, v36, v37
	v_cvt_pk_bf16_f32 v37, v38, v39
	v_cvt_pk_bf16_f32 v38, v32, v33
	v_cvt_pk_bf16_f32 v39, v34, v35
	global_store_dwordx4 v241, v[44:47], s[16:17]
	global_store_dwordx4 v241, v[36:39], s[16:17] offset:256
	v_cvt_pk_fp8_f32 v252, v208, v209
	v_cvt_pk_fp8_f32 v253, v212, v213
	v_cvt_pk_fp8_f32 v242, v216, v217
	v_cvt_pk_fp8_f32 v243, v220, v221
	v_cvt_pk_fp8_f32 v252, v210, v211 op_sel:[0,0,1]
	v_cvt_pk_fp8_f32 v253, v214, v215 op_sel:[0,0,1]
	v_cvt_pk_fp8_f32 v242, v218, v219 op_sel:[0,0,1]
	v_cvt_pk_fp8_f32 v243, v222, v223 op_sel:[0,0,1]
	s_nop 0
	global_store_dwordx2 v254, v[252:253], s[20:21]
	global_store_dwordx2 v254, v[242:243], s[20:21] offset:128
	v_and_b32_e32 v244, 0x7ff, v254
	v_mbcnt_lo_u32_b32 v243, -1, 0
	v_mbcnt_hi_u32_b32 v243, -1, v243
	v_and_b32_e32 v243, 15, v243
	v_lshl_add_u32 v243, v243, 11, v244
	v_lshlrev_b32_e32 v243, 1, v243
	s_nop 1
	s_add_u32 s12, s26, 0x360100
	s_addc_u32 s13, s27, 0
	global_load_dwordx4 v[208:211], v243, s[12:13]
	s_add_u32 s12, s26, 0x330100
	s_addc_u32 s13, s27, 0
	global_load_dwordx4 v[212:215], v243, s[12:13]
	s_add_u32 s12, s26, 0x370100
	s_addc_u32 s13, s27, 0
	global_load_dwordx4 v[216:219], v243, s[12:13]
	s_add_u32 s12, s26, 0x340100
	s_addc_u32 s13, s27, 0
	global_load_dwordx4 v[220:223], v243, s[12:13]
	s_waitcnt vmcnt(32)
	v_pk_add_f32 v[20:21], v[20:21], v[224:225]
	v_pk_add_f32 v[22:23], v[22:23], v[226:227]
	v_pk_add_f32 v[16:17], v[16:17], v[228:229]
	v_pk_add_f32 v[18:19], v[18:19], v[230:231]
	v_pk_add_f32 v[24:25], v[24:25], v[232:233]
	v_pk_add_f32 v[26:27], v[26:27], v[234:235]
	v_pk_add_f32 v[28:29], v[28:29], v[236:237]
	v_pk_add_f32 v[30:31], v[30:31], v[238:239]
	s_add_u32 s16, s38, 0xa0000
	s_addc_u32 s17, s39, 0
	s_add_u32 s20, s60, 0x50000
	s_addc_u32 s21, s61, 0
	v_pk_mul_f32 v[224:225], v[108:109], v[20:21]
	v_pk_mul_f32 v[226:227], v[110:111], v[22:23]
	v_pk_mul_f32 v[228:229], v[104:105], v[16:17]
	v_pk_mul_f32 v[230:231], v[106:107], v[18:19]
	v_pk_mul_f32 v[232:233], v[100:101], v[24:25]
	v_pk_mul_f32 v[234:235], v[102:103], v[26:27]
	v_pk_mul_f32 v[236:237], v[96:97], v[28:29]
	v_pk_mul_f32 v[238:239], v[98:99], v[30:31]
	s_nop 0
	v_cvt_pk_bf16_f32 v20, v20, v21
	v_cvt_pk_bf16_f32 v21, v22, v23
	v_cvt_pk_bf16_f32 v22, v16, v17
	v_cvt_pk_bf16_f32 v23, v18, v19
	v_cvt_pk_bf16_f32 v24, v24, v25
	v_cvt_pk_bf16_f32 v25, v26, v27
	v_cvt_pk_bf16_f32 v26, v28, v29
	v_cvt_pk_bf16_f32 v27, v30, v31
	global_store_dwordx4 v241, v[20:23], s[16:17]
	global_store_dwordx4 v241, v[24:27], s[16:17] offset:256
	v_cvt_pk_fp8_f32 v252, v224, v225
	v_cvt_pk_fp8_f32 v253, v228, v229
	v_cvt_pk_fp8_f32 v242, v232, v233
	v_cvt_pk_fp8_f32 v243, v236, v237
	v_cvt_pk_fp8_f32 v252, v226, v227 op_sel:[0,0,1]
	v_cvt_pk_fp8_f32 v253, v230, v231 op_sel:[0,0,1]
	v_cvt_pk_fp8_f32 v242, v234, v235 op_sel:[0,0,1]
	v_cvt_pk_fp8_f32 v243, v238, v239 op_sel:[0,0,1]
	s_nop 0
	global_store_dwordx2 v254, v[252:253], s[20:21]
	global_store_dwordx2 v254, v[242:243], s[20:21] offset:128
	s_waitcnt vmcnt(28)
	v_pk_add_f32 v[4:5], v[4:5], v[164:165]
	v_pk_add_f32 v[6:7], v[6:7], v[166:167]
	v_pk_add_f32 v[0:1], v[0:1], v[168:169]
	v_pk_add_f32 v[2:3], v[2:3], v[170:171]
	v_pk_add_f32 v[8:9], v[8:9], v[172:173]
	v_pk_add_f32 v[10:11], v[10:11], v[174:175]
	v_pk_add_f32 v[12:13], v[12:13], v[176:177]
	v_pk_add_f32 v[14:15], v[14:15], v[178:179]
	s_add_u32 s16, s38, 0xb0000
	s_addc_u32 s17, s39, 0
	s_add_u32 s20, s60, 0x58000
	s_addc_u32 s21, s61, 0
	v_pk_mul_f32 v[164:165], v[108:109], v[4:5]
	v_pk_mul_f32 v[166:167], v[110:111], v[6:7]
	v_pk_mul_f32 v[168:169], v[104:105], v[0:1]
	v_pk_mul_f32 v[170:171], v[106:107], v[2:3]
	v_pk_mul_f32 v[172:173], v[100:101], v[8:9]
	v_pk_mul_f32 v[174:175], v[102:103], v[10:11]
	v_pk_mul_f32 v[176:177], v[96:97], v[12:13]
	v_pk_mul_f32 v[178:179], v[98:99], v[14:15]
	s_nop 0
	v_cvt_pk_bf16_f32 v4, v4, v5
	v_cvt_pk_bf16_f32 v5, v6, v7
	v_cvt_pk_bf16_f32 v6, v0, v1
	v_cvt_pk_bf16_f32 v7, v2, v3
	v_cvt_pk_bf16_f32 v8, v8, v9
	v_cvt_pk_bf16_f32 v9, v10, v11
	v_cvt_pk_bf16_f32 v10, v12, v13
	v_cvt_pk_bf16_f32 v11, v14, v15
	global_store_dwordx4 v241, v[4:7], s[16:17]
	global_store_dwordx4 v241, v[8:11], s[16:17] offset:256
	v_cvt_pk_fp8_f32 v252, v164, v165
	v_cvt_pk_fp8_f32 v253, v168, v169
	v_cvt_pk_fp8_f32 v242, v172, v173
	v_cvt_pk_fp8_f32 v243, v176, v177
	v_cvt_pk_fp8_f32 v252, v166, v167 op_sel:[0,0,1]
	v_cvt_pk_fp8_f32 v253, v170, v171 op_sel:[0,0,1]
	v_cvt_pk_fp8_f32 v242, v174, v175 op_sel:[0,0,1]
	v_cvt_pk_fp8_f32 v243, v178, v179 op_sel:[0,0,1]
	s_nop 0
	global_store_dwordx2 v254, v[252:253], s[20:21]
	global_store_dwordx2 v254, v[242:243], s[20:21] offset:128
	v_mbcnt_lo_u32_b32 v164, -1, 0
	v_mbcnt_hi_u32_b32 v164, -1, v164
	v_and_b32_e32 v165, 15, v164
	v_lshrrev_b32_e32 v166, 4, v164
	s_lshr_b32 s33, s77, 6
	s_lshr_b32 s41, s78, 5
	s_lshl_b32 s100, s33, 2
	s_add_i32 s100, s100, s41
	v_lshl_add_u32 v167, v166, 2, s77
	v_mul_u32_u24_e32 v167, 48, v167
	v_add_u32_e32 v167, v167, v165
	v_lshlrev_b32_e32 v167, 2, v167
	v_add_u32_e32 v168, s77, v165
	v_lshlrev_b32_e32 v168, 2, v168
	v_lshlrev_b32_e32 v169, 2, v166
	v_sub_u32_e32 v169, v165, v169
	v_cmp_eq_u32_e64 s[12:13], 0, v169
	v_cmp_eq_u32_e64 s[16:17], 1, v169
	v_cmp_eq_u32_e64 s[20:21], 2, v169
	v_cmp_eq_u32_e64 s[22:23], 3, v169
	s_barrier
; __global__ void __launch_bounds__(512, 2) hymba_fwd(Args args) {
;     ...
;                     for (int s4 = 0; s4 < 4; ++s4)
; #pragma unroll
;                         for (int x = 0; x < 2; ++x) { const bf16x8 xh = __builtin_bit_cast(bf16x8, xa[x][s4]);
; #pragma unroll
;                             for (int nt = 0; nt < 3; ++nt) {
;                                 acc[x][nt] = __builtin_amdgcn_mfma_f32_16x16x32_bf16(xh, bl[s4][nt], acc[x][nt], 0, 0, 0);
;                                 acc[x][nt] = __builtin_amdgcn_mfma_f32_16x16x32_bf16(xh, bh[s4][nt], acc[x][nt], 0, 0, 0); } }
;                 }
; #pragma unroll
;                 for (int x = 0; x < 2; ++x) {
; #pragma unroll
;                     for (int nt = 0; nt < 3; ++nt)
; #pragma unroll
;                         for (int e = 0; e < 4; ++e) part[(wave * 32 + 16 * x + 4 * kg + e) * 48 + 16 * nt + li] = acc[x][nt][e];
;                     float s1 = ss[x]; s1 += __shfl_xor(s1, 16); s1 += __shfl_xor(s1, 32);
;                     if (kg == 0) ssp[wave * 32 + 16 * x + li] = s1; }
	v_mov_b32_e32 v172, 0
	v_mov_b32_e32 v173, 0
	v_mov_b32_e32 v174, 0
	v_mov_b32_e32 v175, 0
	s_mul_i32 s101, s100, 0x1800
	v_lshl_add_u32 v170, v164, 4, s101
	ds_write_b128 v170, v[172:175] offset:0
	ds_write_b128 v170, v[172:175] offset:1024
	ds_write_b128 v170, v[172:175] offset:2048
	ds_write_b128 v170, v[172:175] offset:3072
	ds_write_b128 v170, v[172:175] offset:4096
	ds_write_b128 v170, v[172:175] offset:5120
	s_lshl_b32 s101, s100, 7
	v_lshl_add_u32 v171, v164, 2, s101
	s_mov_b32 exec_lo, -1
	s_mov_b32 exec_hi, 0
	ds_write_b32 v171, v172 offset:49152
	s_mov_b64 exec, -1
	s_waitcnt vmcnt(8) lgkmcnt(0)
	s_barrier
	v_mov_b32_e32 v176, 0x4b800000
	v_mov_b32_e32 v177, 0x47800000
	v_mfma_f32_16x16x32_bf16 v[224:227], v[140:143], v[180:183], 0
	v_mfma_f32_16x16x32_bf16 v[224:227], v[140:143], v[184:187], v[224:227]
	v_mfma_f32_16x16x32_bf16 v[224:227], v[132:135], v[204:207], v[224:227]
	v_mfma_f32_16x16x32_bf16 v[224:227], v[132:135], v[148:151], v[224:227]
	v_mfma_f32_16x16x32_bf16 v[228:231], v[140:143], v[188:191], 0
	v_mfma_f32_16x16x32_bf16 v[228:231], v[140:143], v[192:195], v[228:231]
	v_mfma_f32_16x16x32_bf16 v[228:231], v[132:135], v[208:211], v[228:231]
	v_mfma_f32_16x16x32_bf16 v[228:231], v[132:135], v[212:215], v[228:231]
	v_mfma_f32_16x16x32_bf16 v[232:235], v[140:143], v[196:199], 0
	v_mfma_f32_16x16x32_bf16 v[232:235], v[140:143], v[200:203], v[232:235]
	v_mfma_f32_16x16x32_bf16 v[232:235], v[132:135], v[216:219], v[232:235]
	v_mfma_f32_16x16x32_bf16 v[232:235], v[132:135], v[220:223], v[232:235]
	v_mfma_f32_16x16x32_bf16 v[236:239], v[140:143], v[140:143], 0
	v_mfma_f32_16x16x32_bf16 v[236:239], v[132:135], v[132:135], v[236:239]
	s_nop 7
	s_nop 3
	v_mul_f32_e32 v224, v224, v176
	v_cvt_i32_f32_e32 v224, v224
	v_mul_f32_e32 v225, v225, v176
	v_cvt_i32_f32_e32 v225, v225
	v_mul_f32_e32 v226, v226, v176
	v_cvt_i32_f32_e32 v226, v226
	v_mul_f32_e32 v227, v227, v176
	v_cvt_i32_f32_e32 v227, v227
	v_mul_f32_e32 v228, v228, v176
	v_cvt_i32_f32_e32 v228, v228
	v_mul_f32_e32 v229, v229, v176
	v_cvt_i32_f32_e32 v229, v229
	v_mul_f32_e32 v230, v230, v176
	v_cvt_i32_f32_e32 v230, v230
	v_mul_f32_e32 v231, v231, v176
	v_cvt_i32_f32_e32 v231, v231
	v_mul_f32_e32 v232, v232, v176
	v_cvt_i32_f32_e32 v232, v232
	v_mul_f32_e32 v233, v233, v176
	v_cvt_i32_f32_e32 v233, v233
	v_mul_f32_e32 v234, v234, v176
	v_cvt_i32_f32_e32 v234, v234
	v_mul_f32_e32 v235, v235, v176
	v_cvt_i32_f32_e32 v235, v235
	v_mul_f32_e32 v236, v236, v177
	v_cvt_i32_f32_e32 v236, v236
	v_mul_f32_e32 v237, v237, v177
	v_cvt_i32_f32_e32 v237, v237
	v_mul_f32_e32 v238, v238, v177
	v_cvt_i32_f32_e32 v238, v238
	v_mul_f32_e32 v239, v239, v177
	v_cvt_i32_f32_e32 v239, v239
	ds_add_u32 v167, v224 offset:0
	ds_add_u32 v167, v225 offset:192
	ds_add_u32 v167, v226 offset:384
	ds_add_u32 v167, v227 offset:576
	ds_add_u32 v167, v228 offset:64
	ds_add_u32 v167, v229 offset:256
	ds_add_u32 v167, v230 offset:448
	ds_add_u32 v167, v231 offset:640
	ds_add_u32 v167, v232 offset:128
	ds_add_u32 v167, v233 offset:320
	ds_add_u32 v167, v234 offset:512
	ds_add_u32 v167, v235 offset:704
	s_mov_b64 exec, s[12:13]
	ds_add_u32 v168, v236 offset:49152
	s_mov_b64 exec, s[16:17]
	ds_add_u32 v168, v237 offset:49152
	s_mov_b64 exec, s[20:21]
	ds_add_u32 v168, v238 offset:49152
	s_mov_b64 exec, s[22:23]
	ds_add_u32 v168, v239 offset:49152
	s_mov_b64 exec, -1
	v_mfma_f32_16x16x32_bf16 v[224:227], v[124:127], v[180:183], 0
	v_mfma_f32_16x16x32_bf16 v[224:227], v[124:127], v[184:187], v[224:227]
	v_mfma_f32_16x16x32_bf16 v[224:227], v[116:119], v[204:207], v[224:227]
	v_mfma_f32_16x16x32_bf16 v[224:227], v[116:119], v[148:151], v[224:227]
	v_mfma_f32_16x16x32_bf16 v[228:231], v[124:127], v[188:191], 0
	v_mfma_f32_16x16x32_bf16 v[228:231], v[124:127], v[192:195], v[228:231]
	v_mfma_f32_16x16x32_bf16 v[228:231], v[116:119], v[208:211], v[228:231]
	v_mfma_f32_16x16x32_bf16 v[228:231], v[116:119], v[212:215], v[228:231]
	v_mfma_f32_16x16x32_bf16 v[232:235], v[124:127], v[196:199], 0
	v_mfma_f32_16x16x32_bf16 v[232:235], v[124:127], v[200:203], v[232:235]
	v_mfma_f32_16x16x32_bf16 v[232:235], v[116:119], v[216:219], v[232:235]
	v_mfma_f32_16x16x32_bf16 v[232:235], v[116:119], v[220:223], v[232:235]
	v_mfma_f32_16x16x32_bf16 v[236:239], v[124:127], v[124:127], 0
	v_mfma_f32_16x16x32_bf16 v[236:239], v[116:119], v[116:119], v[236:239]
	s_nop 7
	s_nop 3
	v_mul_f32_e32 v224, v224, v176
	v_cvt_i32_f32_e32 v224, v224
	v_mul_f32_e32 v225, v225, v176
	v_cvt_i32_f32_e32 v225, v225
	v_mul_f32_e32 v226, v226, v176
	v_cvt_i32_f32_e32 v226, v226
	v_mul_f32_e32 v227, v227, v176
	v_cvt_i32_f32_e32 v227, v227
	v_mul_f32_e32 v228, v228, v176
	v_cvt_i32_f32_e32 v228, v228
	v_mul_f32_e32 v229, v229, v176
	v_cvt_i32_f32_e32 v229, v229
	v_mul_f32_e32 v230, v230, v176
	v_cvt_i32_f32_e32 v230, v230
	v_mul_f32_e32 v231, v231, v176
	v_cvt_i32_f32_e32 v231, v231
	v_mul_f32_e32 v232, v232, v176
	v_cvt_i32_f32_e32 v232, v232
	v_mul_f32_e32 v233, v233, v176
	v_cvt_i32_f32_e32 v233, v233
	v_mul_f32_e32 v234, v234, v176
	v_cvt_i32_f32_e32 v234, v234
	v_mul_f32_e32 v235, v235, v176
	v_cvt_i32_f32_e32 v235, v235
	v_mul_f32_e32 v236, v236, v177
	v_cvt_i32_f32_e32 v236, v236
	v_mul_f32_e32 v237, v237, v177
	v_cvt_i32_f32_e32 v237, v237
	v_mul_f32_e32 v238, v238, v177
	v_cvt_i32_f32_e32 v238, v238
	v_mul_f32_e32 v239, v239, v177
	v_cvt_i32_f32_e32 v239, v239
	ds_add_u32 v167, v224 offset:3072
	ds_add_u32 v167, v225 offset:3264
	ds_add_u32 v167, v226 offset:3456
	ds_add_u32 v167, v227 offset:3648
	ds_add_u32 v167, v228 offset:3136
	ds_add_u32 v167, v229 offset:3328
	ds_add_u32 v167, v230 offset:3520
	ds_add_u32 v167, v231 offset:3712
; __global__ void __launch_bounds__(512, 2) hymba_fwd(Args args) {
;     ...
;                     for (int s4 = 0; s4 < 4; ++s4)
; #pragma unroll
;                         for (int x = 0; x < 2; ++x) { const bf16x8 xh = __builtin_bit_cast(bf16x8, xa[x][s4]);
; #pragma unroll
;                             for (int nt = 0; nt < 3; ++nt) {
;                                 acc[x][nt] = __builtin_amdgcn_mfma_f32_16x16x32_bf16(xh, bl[s4][nt], acc[x][nt], 0, 0, 0);
;                                 acc[x][nt] = __builtin_amdgcn_mfma_f32_16x16x32_bf16(xh, bh[s4][nt], acc[x][nt], 0, 0, 0); } }
;                 }
; #pragma unroll
;                 for (int x = 0; x < 2; ++x) {
; #pragma unroll
;                     for (int nt = 0; nt < 3; ++nt)
; #pragma unroll
;                         for (int e = 0; e < 4; ++e) part[(wave * 32 + 16 * x + 4 * kg + e) * 48 + 16 * nt + li] = acc[x][nt][e];
;                     float s1 = ss[x]; s1 += __shfl_xor(s1, 16); s1 += __shfl_xor(s1, 32);
;                     if (kg == 0) ssp[wave * 32 + 16 * x + li] = s1; }
	ds_add_u32 v167, v232 offset:3200
	ds_add_u32 v167, v233 offset:3392
	ds_add_u32 v167, v234 offset:3584
	ds_add_u32 v167, v235 offset:3776
	s_mov_b64 exec, s[12:13]
	ds_add_u32 v168, v236 offset:49216
	s_mov_b64 exec, s[16:17]
	ds_add_u32 v168, v237 offset:49216
	s_mov_b64 exec, s[20:21]
	ds_add_u32 v168, v238 offset:49216
	s_mov_b64 exec, s[22:23]
	ds_add_u32 v168, v239 offset:49216
	s_mov_b64 exec, -1
	v_mfma_f32_16x16x32_bf16 v[224:227], v[92:95], v[180:183], 0
	v_mfma_f32_16x16x32_bf16 v[224:227], v[92:95], v[184:187], v[224:227]
	v_mfma_f32_16x16x32_bf16 v[224:227], v[84:87], v[204:207], v[224:227]
	v_mfma_f32_16x16x32_bf16 v[224:227], v[84:87], v[148:151], v[224:227]
	v_mfma_f32_16x16x32_bf16 v[228:231], v[92:95], v[188:191], 0
	v_mfma_f32_16x16x32_bf16 v[228:231], v[92:95], v[192:195], v[228:231]
	v_mfma_f32_16x16x32_bf16 v[228:231], v[84:87], v[208:211], v[228:231]
	v_mfma_f32_16x16x32_bf16 v[228:231], v[84:87], v[212:215], v[228:231]
	v_mfma_f32_16x16x32_bf16 v[232:235], v[92:95], v[196:199], 0
	v_mfma_f32_16x16x32_bf16 v[232:235], v[92:95], v[200:203], v[232:235]
	v_mfma_f32_16x16x32_bf16 v[232:235], v[84:87], v[216:219], v[232:235]
	v_mfma_f32_16x16x32_bf16 v[232:235], v[84:87], v[220:223], v[232:235]
	v_mfma_f32_16x16x32_bf16 v[236:239], v[92:95], v[92:95], 0
	v_mfma_f32_16x16x32_bf16 v[236:239], v[84:87], v[84:87], v[236:239]
	s_nop 7
	s_nop 3
	v_mul_f32_e32 v224, v224, v176
	v_cvt_i32_f32_e32 v224, v224
	v_mul_f32_e32 v225, v225, v176
	v_cvt_i32_f32_e32 v225, v225
	v_mul_f32_e32 v226, v226, v176
	v_cvt_i32_f32_e32 v226, v226
	v_mul_f32_e32 v227, v227, v176
	v_cvt_i32_f32_e32 v227, v227
	v_mul_f32_e32 v228, v228, v176
	v_cvt_i32_f32_e32 v228, v228
	v_mul_f32_e32 v229, v229, v176
	v_cvt_i32_f32_e32 v229, v229
	v_mul_f32_e32 v230, v230, v176
	v_cvt_i32_f32_e32 v230, v230
	v_mul_f32_e32 v231, v231, v176
	v_cvt_i32_f32_e32 v231, v231
	v_mul_f32_e32 v232, v232, v176
	v_cvt_i32_f32_e32 v232, v232
	v_mul_f32_e32 v233, v233, v176
	v_cvt_i32_f32_e32 v233, v233
	v_mul_f32_e32 v234, v234, v176
	v_cvt_i32_f32_e32 v234, v234
	v_mul_f32_e32 v235, v235, v176
	v_cvt_i32_f32_e32 v235, v235
	v_mul_f32_e32 v236, v236, v177
	v_cvt_i32_f32_e32 v236, v236
	v_mul_f32_e32 v237, v237, v177
	v_cvt_i32_f32_e32 v237, v237
	v_mul_f32_e32 v238, v238, v177
	v_cvt_i32_f32_e32 v238, v238
	v_mul_f32_e32 v239, v239, v177
	v_cvt_i32_f32_e32 v239, v239
	ds_add_u32 v167, v224 offset:6144
	ds_add_u32 v167, v225 offset:6336
	ds_add_u32 v167, v226 offset:6528
	ds_add_u32 v167, v227 offset:6720
	ds_add_u32 v167, v228 offset:6208
	ds_add_u32 v167, v229 offset:6400
	ds_add_u32 v167, v230 offset:6592
	ds_add_u32 v167, v231 offset:6784
	ds_add_u32 v167, v232 offset:6272
	ds_add_u32 v167, v233 offset:6464
	ds_add_u32 v167, v234 offset:6656
	ds_add_u32 v167, v235 offset:6848
	s_mov_b64 exec, s[12:13]
	ds_add_u32 v168, v236 offset:49280
	s_mov_b64 exec, s[16:17]
	ds_add_u32 v168, v237 offset:49280
	s_mov_b64 exec, s[20:21]
	ds_add_u32 v168, v238 offset:49280
	s_mov_b64 exec, s[22:23]
	ds_add_u32 v168, v239 offset:49280
	s_mov_b64 exec, -1
	v_mfma_f32_16x16x32_bf16 v[224:227], v[76:79], v[180:183], 0
	v_mfma_f32_16x16x32_bf16 v[224:227], v[76:79], v[184:187], v[224:227]
	v_mfma_f32_16x16x32_bf16 v[224:227], v[68:71], v[204:207], v[224:227]
	v_mfma_f32_16x16x32_bf16 v[224:227], v[68:71], v[148:151], v[224:227]
	v_mfma_f32_16x16x32_bf16 v[228:231], v[76:79], v[188:191], 0
	v_mfma_f32_16x16x32_bf16 v[228:231], v[76:79], v[192:195], v[228:231]
	v_mfma_f32_16x16x32_bf16 v[228:231], v[68:71], v[208:211], v[228:231]
	v_mfma_f32_16x16x32_bf16 v[228:231], v[68:71], v[212:215], v[228:231]
	v_mfma_f32_16x16x32_bf16 v[232:235], v[76:79], v[196:199], 0
	v_mfma_f32_16x16x32_bf16 v[232:235], v[76:79], v[200:203], v[232:235]
	v_mfma_f32_16x16x32_bf16 v[232:235], v[68:71], v[216:219], v[232:235]
	v_mfma_f32_16x16x32_bf16 v[232:235], v[68:71], v[220:223], v[232:235]
	v_mfma_f32_16x16x32_bf16 v[236:239], v[76:79], v[76:79], 0
	v_mfma_f32_16x16x32_bf16 v[236:239], v[68:71], v[68:71], v[236:239]
	s_nop 7
	s_nop 3
	v_mul_f32_e32 v224, v224, v176
	v_cvt_i32_f32_e32 v224, v224
	v_mul_f32_e32 v225, v225, v176
	v_cvt_i32_f32_e32 v225, v225
	v_mul_f32_e32 v226, v226, v176
	v_cvt_i32_f32_e32 v226, v226
	v_mul_f32_e32 v227, v227, v176
	v_cvt_i32_f32_e32 v227, v227
	v_mul_f32_e32 v228, v228, v176
	v_cvt_i32_f32_e32 v228, v228
	v_mul_f32_e32 v229, v229, v176
	v_cvt_i32_f32_e32 v229, v229
	v_mul_f32_e32 v230, v230, v176
	v_cvt_i32_f32_e32 v230, v230
	v_mul_f32_e32 v231, v231, v176
	v_cvt_i32_f32_e32 v231, v231
	v_mul_f32_e32 v232, v232, v176
	v_cvt_i32_f32_e32 v232, v232
	v_mul_f32_e32 v233, v233, v176
	v_cvt_i32_f32_e32 v233, v233
	v_mul_f32_e32 v234, v234, v176
	v_cvt_i32_f32_e32 v234, v234
	v_mul_f32_e32 v235, v235, v176
	v_cvt_i32_f32_e32 v235, v235
	v_mul_f32_e32 v236, v236, v177
	v_cvt_i32_f32_e32 v236, v236
	v_mul_f32_e32 v237, v237, v177
	v_cvt_i32_f32_e32 v237, v237
	v_mul_f32_e32 v238, v238, v177
	v_cvt_i32_f32_e32 v238, v238
	v_mul_f32_e32 v239, v239, v177
	v_cvt_i32_f32_e32 v239, v239
	ds_add_u32 v167, v224 offset:9216
	ds_add_u32 v167, v225 offset:9408
	ds_add_u32 v167, v226 offset:9600
	ds_add_u32 v167, v227 offset:9792
	ds_add_u32 v167, v228 offset:9280
	ds_add_u32 v167, v229 offset:9472
	ds_add_u32 v167, v230 offset:9664
	ds_add_u32 v167, v231 offset:9856
	ds_add_u32 v167, v232 offset:9344
	ds_add_u32 v167, v233 offset:9536
	ds_add_u32 v167, v234 offset:9728
	ds_add_u32 v167, v235 offset:9920
	s_mov_b64 exec, s[12:13]
	ds_add_u32 v168, v236 offset:49344
	s_mov_b64 exec, s[16:17]
	ds_add_u32 v168, v237 offset:49344
	s_mov_b64 exec, s[20:21]
	ds_add_u32 v168, v238 offset:49344
; __global__ void __launch_bounds__(512, 2) hymba_fwd(Args args) {
;     ...
;                     for (int s4 = 0; s4 < 4; ++s4)
; #pragma unroll
;                         for (int x = 0; x < 2; ++x) { const bf16x8 xh = __builtin_bit_cast(bf16x8, xa[x][s4]);
; #pragma unroll
;                             for (int nt = 0; nt < 3; ++nt) {
;                                 acc[x][nt] = __builtin_amdgcn_mfma_f32_16x16x32_bf16(xh, bl[s4][nt], acc[x][nt], 0, 0, 0);
;                                 acc[x][nt] = __builtin_amdgcn_mfma_f32_16x16x32_bf16(xh, bh[s4][nt], acc[x][nt], 0, 0, 0); } }
;                 }
; #pragma unroll
;                 for (int x = 0; x < 2; ++x) {
; #pragma unroll
;                     for (int nt = 0; nt < 3; ++nt)
; #pragma unroll
;                         for (int e = 0; e < 4; ++e) part[(wave * 32 + 16 * x + 4 * kg + e) * 48 + 16 * nt + li] = acc[x][nt][e];
;                     float s1 = ss[x]; s1 += __shfl_xor(s1, 16); s1 += __shfl_xor(s1, 32);
;                     if (kg == 0) ssp[wave * 32 + 16 * x + li] = s1; }
	s_mov_b64 exec, s[22:23]
	ds_add_u32 v168, v239 offset:49344
	s_mov_b64 exec, -1
	v_mfma_f32_16x16x32_bf16 v[224:227], v[60:63], v[180:183], 0
	v_mfma_f32_16x16x32_bf16 v[224:227], v[60:63], v[184:187], v[224:227]
	v_mfma_f32_16x16x32_bf16 v[224:227], v[52:55], v[204:207], v[224:227]
	v_mfma_f32_16x16x32_bf16 v[224:227], v[52:55], v[148:151], v[224:227]
	v_mfma_f32_16x16x32_bf16 v[228:231], v[60:63], v[188:191], 0
	v_mfma_f32_16x16x32_bf16 v[228:231], v[60:63], v[192:195], v[228:231]
	v_mfma_f32_16x16x32_bf16 v[228:231], v[52:55], v[208:211], v[228:231]
	v_mfma_f32_16x16x32_bf16 v[228:231], v[52:55], v[212:215], v[228:231]
	v_mfma_f32_16x16x32_bf16 v[232:235], v[60:63], v[196:199], 0
	v_mfma_f32_16x16x32_bf16 v[232:235], v[60:63], v[200:203], v[232:235]
	v_mfma_f32_16x16x32_bf16 v[232:235], v[52:55], v[216:219], v[232:235]
	v_mfma_f32_16x16x32_bf16 v[232:235], v[52:55], v[220:223], v[232:235]
	v_mfma_f32_16x16x32_bf16 v[236:239], v[60:63], v[60:63], 0
	v_mfma_f32_16x16x32_bf16 v[236:239], v[52:55], v[52:55], v[236:239]
	s_nop 7
	s_nop 3
	v_mul_f32_e32 v224, v224, v176
	v_cvt_i32_f32_e32 v224, v224
	v_mul_f32_e32 v225, v225, v176
	v_cvt_i32_f32_e32 v225, v225
	v_mul_f32_e32 v226, v226, v176
	v_cvt_i32_f32_e32 v226, v226
	v_mul_f32_e32 v227, v227, v176
	v_cvt_i32_f32_e32 v227, v227
	v_mul_f32_e32 v228, v228, v176
	v_cvt_i32_f32_e32 v228, v228
	v_mul_f32_e32 v229, v229, v176
	v_cvt_i32_f32_e32 v229, v229
	v_mul_f32_e32 v230, v230, v176
	v_cvt_i32_f32_e32 v230, v230
	v_mul_f32_e32 v231, v231, v176
	v_cvt_i32_f32_e32 v231, v231
	v_mul_f32_e32 v232, v232, v176
	v_cvt_i32_f32_e32 v232, v232
	v_mul_f32_e32 v233, v233, v176
	v_cvt_i32_f32_e32 v233, v233
	v_mul_f32_e32 v234, v234, v176
	v_cvt_i32_f32_e32 v234, v234
	v_mul_f32_e32 v235, v235, v176
	v_cvt_i32_f32_e32 v235, v235
	v_mul_f32_e32 v236, v236, v177
	v_cvt_i32_f32_e32 v236, v236
	v_mul_f32_e32 v237, v237, v177
	v_cvt_i32_f32_e32 v237, v237
	v_mul_f32_e32 v238, v238, v177
	v_cvt_i32_f32_e32 v238, v238
	v_mul_f32_e32 v239, v239, v177
	v_cvt_i32_f32_e32 v239, v239
	ds_add_u32 v167, v224 offset:24576
	ds_add_u32 v167, v225 offset:24768
	ds_add_u32 v167, v226 offset:24960
	ds_add_u32 v167, v227 offset:25152
	ds_add_u32 v167, v228 offset:24640
	ds_add_u32 v167, v229 offset:24832
	ds_add_u32 v167, v230 offset:25024
	ds_add_u32 v167, v231 offset:25216
	ds_add_u32 v167, v232 offset:24704
	ds_add_u32 v167, v233 offset:24896
	ds_add_u32 v167, v234 offset:25088
	ds_add_u32 v167, v235 offset:25280
	s_mov_b64 exec, s[12:13]
	ds_add_u32 v168, v236 offset:49664
	s_mov_b64 exec, s[16:17]
	ds_add_u32 v168, v237 offset:49664
	s_mov_b64 exec, s[20:21]
	ds_add_u32 v168, v238 offset:49664
	s_mov_b64 exec, s[22:23]
	ds_add_u32 v168, v239 offset:49664
	s_mov_b64 exec, -1
	v_mfma_f32_16x16x32_bf16 v[224:227], v[44:47], v[180:183], 0
	v_mfma_f32_16x16x32_bf16 v[224:227], v[44:47], v[184:187], v[224:227]
	v_mfma_f32_16x16x32_bf16 v[224:227], v[36:39], v[204:207], v[224:227]
	v_mfma_f32_16x16x32_bf16 v[224:227], v[36:39], v[148:151], v[224:227]
	v_mfma_f32_16x16x32_bf16 v[228:231], v[44:47], v[188:191], 0
	v_mfma_f32_16x16x32_bf16 v[228:231], v[44:47], v[192:195], v[228:231]
	v_mfma_f32_16x16x32_bf16 v[228:231], v[36:39], v[208:211], v[228:231]
	v_mfma_f32_16x16x32_bf16 v[228:231], v[36:39], v[212:215], v[228:231]
	v_mfma_f32_16x16x32_bf16 v[232:235], v[44:47], v[196:199], 0
	v_mfma_f32_16x16x32_bf16 v[232:235], v[44:47], v[200:203], v[232:235]
	v_mfma_f32_16x16x32_bf16 v[232:235], v[36:39], v[216:219], v[232:235]
	v_mfma_f32_16x16x32_bf16 v[232:235], v[36:39], v[220:223], v[232:235]
	v_mfma_f32_16x16x32_bf16 v[236:239], v[44:47], v[44:47], 0
	v_mfma_f32_16x16x32_bf16 v[236:239], v[36:39], v[36:39], v[236:239]
	s_nop 7
	s_nop 3
	v_mul_f32_e32 v224, v224, v176
	v_cvt_i32_f32_e32 v224, v224
	v_mul_f32_e32 v225, v225, v176
	v_cvt_i32_f32_e32 v225, v225
	v_mul_f32_e32 v226, v226, v176
	v_cvt_i32_f32_e32 v226, v226
	v_mul_f32_e32 v227, v227, v176
	v_cvt_i32_f32_e32 v227, v227
	v_mul_f32_e32 v228, v228, v176
	v_cvt_i32_f32_e32 v228, v228
	v_mul_f32_e32 v229, v229, v176
	v_cvt_i32_f32_e32 v229, v229
	v_mul_f32_e32 v230, v230, v176
	v_cvt_i32_f32_e32 v230, v230
	v_mul_f32_e32 v231, v231, v176
	v_cvt_i32_f32_e32 v231, v231
	v_mul_f32_e32 v232, v232, v176
	v_cvt_i32_f32_e32 v232, v232
	v_mul_f32_e32 v233, v233, v176
	v_cvt_i32_f32_e32 v233, v233
	v_mul_f32_e32 v234, v234, v176
	v_cvt_i32_f32_e32 v234, v234
	v_mul_f32_e32 v235, v235, v176
	v_cvt_i32_f32_e32 v235, v235
	v_mul_f32_e32 v236, v236, v177
	v_cvt_i32_f32_e32 v236, v236
	v_mul_f32_e32 v237, v237, v177
	v_cvt_i32_f32_e32 v237, v237
	v_mul_f32_e32 v238, v238, v177
	v_cvt_i32_f32_e32 v238, v238
	v_mul_f32_e32 v239, v239, v177
	v_cvt_i32_f32_e32 v239, v239
	ds_add_u32 v167, v224 offset:27648
	ds_add_u32 v167, v225 offset:27840
	ds_add_u32 v167, v226 offset:28032
	ds_add_u32 v167, v227 offset:28224
	ds_add_u32 v167, v228 offset:27712
	ds_add_u32 v167, v229 offset:27904
	ds_add_u32 v167, v230 offset:28096
	ds_add_u32 v167, v231 offset:28288
	ds_add_u32 v167, v232 offset:27776
	ds_add_u32 v167, v233 offset:27968
	ds_add_u32 v167, v234 offset:28160
	ds_add_u32 v167, v235 offset:28352
	s_mov_b64 exec, s[12:13]
	ds_add_u32 v168, v236 offset:49728
	s_mov_b64 exec, s[16:17]
	ds_add_u32 v168, v237 offset:49728
	s_mov_b64 exec, s[20:21]
	ds_add_u32 v168, v238 offset:49728
	s_mov_b64 exec, s[22:23]
	ds_add_u32 v168, v239 offset:49728
	s_mov_b64 exec, -1
	v_mfma_f32_16x16x32_bf16 v[224:227], v[20:23], v[180:183], 0
	v_mfma_f32_16x16x32_bf16 v[224:227], v[20:23], v[184:187], v[224:227]
	v_mfma_f32_16x16x32_bf16 v[224:227], v[24:27], v[204:207], v[224:227]
; __global__ void __launch_bounds__(512, 2) hymba_fwd(Args args) {
;     ...
;                     for (int s4 = 0; s4 < 4; ++s4)
; #pragma unroll
;                         for (int x = 0; x < 2; ++x) { const bf16x8 xh = __builtin_bit_cast(bf16x8, xa[x][s4]);
; #pragma unroll
;                             for (int nt = 0; nt < 3; ++nt) {
;                                 acc[x][nt] = __builtin_amdgcn_mfma_f32_16x16x32_bf16(xh, bl[s4][nt], acc[x][nt], 0, 0, 0);
;                                 acc[x][nt] = __builtin_amdgcn_mfma_f32_16x16x32_bf16(xh, bh[s4][nt], acc[x][nt], 0, 0, 0); } }
;                 }
; #pragma unroll
;                 for (int x = 0; x < 2; ++x) {
; #pragma unroll
;                     for (int nt = 0; nt < 3; ++nt)
; #pragma unroll
;                         for (int e = 0; e < 4; ++e) part[(wave * 32 + 16 * x + 4 * kg + e) * 48 + 16 * nt + li] = acc[x][nt][e];
;                     float s1 = ss[x]; s1 += __shfl_xor(s1, 16); s1 += __shfl_xor(s1, 32);
;                     if (kg == 0) ssp[wave * 32 + 16 * x + li] = s1; }
	v_mfma_f32_16x16x32_bf16 v[224:227], v[24:27], v[148:151], v[224:227]
	v_mfma_f32_16x16x32_bf16 v[228:231], v[20:23], v[188:191], 0
	v_mfma_f32_16x16x32_bf16 v[228:231], v[20:23], v[192:195], v[228:231]
	v_mfma_f32_16x16x32_bf16 v[228:231], v[24:27], v[208:211], v[228:231]
	v_mfma_f32_16x16x32_bf16 v[228:231], v[24:27], v[212:215], v[228:231]
	v_mfma_f32_16x16x32_bf16 v[232:235], v[20:23], v[196:199], 0
	v_mfma_f32_16x16x32_bf16 v[232:235], v[20:23], v[200:203], v[232:235]
	v_mfma_f32_16x16x32_bf16 v[232:235], v[24:27], v[216:219], v[232:235]
	v_mfma_f32_16x16x32_bf16 v[232:235], v[24:27], v[220:223], v[232:235]
	v_mfma_f32_16x16x32_bf16 v[236:239], v[20:23], v[20:23], 0
	v_mfma_f32_16x16x32_bf16 v[236:239], v[24:27], v[24:27], v[236:239]
	s_nop 7
	s_nop 3
	v_mul_f32_e32 v224, v224, v176
	v_cvt_i32_f32_e32 v224, v224
	v_mul_f32_e32 v225, v225, v176
	v_cvt_i32_f32_e32 v225, v225
	v_mul_f32_e32 v226, v226, v176
	v_cvt_i32_f32_e32 v226, v226
	v_mul_f32_e32 v227, v227, v176
	v_cvt_i32_f32_e32 v227, v227
	v_mul_f32_e32 v228, v228, v176
	v_cvt_i32_f32_e32 v228, v228
	v_mul_f32_e32 v229, v229, v176
	v_cvt_i32_f32_e32 v229, v229
	v_mul_f32_e32 v230, v230, v176
	v_cvt_i32_f32_e32 v230, v230
	v_mul_f32_e32 v231, v231, v176
	v_cvt_i32_f32_e32 v231, v231
	v_mul_f32_e32 v232, v232, v176
	v_cvt_i32_f32_e32 v232, v232
	v_mul_f32_e32 v233, v233, v176
	v_cvt_i32_f32_e32 v233, v233
	v_mul_f32_e32 v234, v234, v176
	v_cvt_i32_f32_e32 v234, v234
	v_mul_f32_e32 v235, v235, v176
	v_cvt_i32_f32_e32 v235, v235
	v_mul_f32_e32 v236, v236, v177
	v_cvt_i32_f32_e32 v236, v236
	v_mul_f32_e32 v237, v237, v177
	v_cvt_i32_f32_e32 v237, v237
	v_mul_f32_e32 v238, v238, v177
	v_cvt_i32_f32_e32 v238, v238
	v_mul_f32_e32 v239, v239, v177
	v_cvt_i32_f32_e32 v239, v239
	ds_add_u32 v167, v224 offset:30720
	ds_add_u32 v167, v225 offset:30912
	ds_add_u32 v167, v226 offset:31104
	ds_add_u32 v167, v227 offset:31296
	ds_add_u32 v167, v228 offset:30784
	ds_add_u32 v167, v229 offset:30976
	ds_add_u32 v167, v230 offset:31168
	ds_add_u32 v167, v231 offset:31360
	ds_add_u32 v167, v232 offset:30848
	ds_add_u32 v167, v233 offset:31040
	ds_add_u32 v167, v234 offset:31232
	ds_add_u32 v167, v235 offset:31424
	s_mov_b64 exec, s[12:13]
	ds_add_u32 v168, v236 offset:49792
	s_mov_b64 exec, s[16:17]
	ds_add_u32 v168, v237 offset:49792
	s_mov_b64 exec, s[20:21]
	ds_add_u32 v168, v238 offset:49792
	s_mov_b64 exec, s[22:23]
	ds_add_u32 v168, v239 offset:49792
	s_mov_b64 exec, -1
	v_mfma_f32_16x16x32_bf16 v[224:227], v[4:7], v[180:183], 0
	v_mfma_f32_16x16x32_bf16 v[224:227], v[4:7], v[184:187], v[224:227]
	v_mfma_f32_16x16x32_bf16 v[224:227], v[8:11], v[204:207], v[224:227]
	v_mfma_f32_16x16x32_bf16 v[224:227], v[8:11], v[148:151], v[224:227]
	v_mfma_f32_16x16x32_bf16 v[228:231], v[4:7], v[188:191], 0
	v_mfma_f32_16x16x32_bf16 v[228:231], v[4:7], v[192:195], v[228:231]
	v_mfma_f32_16x16x32_bf16 v[228:231], v[8:11], v[208:211], v[228:231]
	v_mfma_f32_16x16x32_bf16 v[228:231], v[8:11], v[212:215], v[228:231]
	v_mfma_f32_16x16x32_bf16 v[232:235], v[4:7], v[196:199], 0
	v_mfma_f32_16x16x32_bf16 v[232:235], v[4:7], v[200:203], v[232:235]
	v_mfma_f32_16x16x32_bf16 v[232:235], v[8:11], v[216:219], v[232:235]
	v_mfma_f32_16x16x32_bf16 v[232:235], v[8:11], v[220:223], v[232:235]
	v_mfma_f32_16x16x32_bf16 v[236:239], v[4:7], v[4:7], 0
	v_mfma_f32_16x16x32_bf16 v[236:239], v[8:11], v[8:11], v[236:239]
	s_nop 7
	s_nop 3
	v_mul_f32_e32 v224, v224, v176
	v_cvt_i32_f32_e32 v224, v224
	v_mul_f32_e32 v225, v225, v176
	v_cvt_i32_f32_e32 v225, v225
	v_mul_f32_e32 v226, v226, v176
	v_cvt_i32_f32_e32 v226, v226
	v_mul_f32_e32 v227, v227, v176
	v_cvt_i32_f32_e32 v227, v227
	v_mul_f32_e32 v228, v228, v176
	v_cvt_i32_f32_e32 v228, v228
	v_mul_f32_e32 v229, v229, v176
	v_cvt_i32_f32_e32 v229, v229
	v_mul_f32_e32 v230, v230, v176
	v_cvt_i32_f32_e32 v230, v230
	v_mul_f32_e32 v231, v231, v176
	v_cvt_i32_f32_e32 v231, v231
	v_mul_f32_e32 v232, v232, v176
	v_cvt_i32_f32_e32 v232, v232
	v_mul_f32_e32 v233, v233, v176
	v_cvt_i32_f32_e32 v233, v233
	v_mul_f32_e32 v234, v234, v176
	v_cvt_i32_f32_e32 v234, v234
	v_mul_f32_e32 v235, v235, v176
	v_cvt_i32_f32_e32 v235, v235
	v_mul_f32_e32 v236, v236, v177
	v_cvt_i32_f32_e32 v236, v236
	v_mul_f32_e32 v237, v237, v177
	v_cvt_i32_f32_e32 v237, v237
	v_mul_f32_e32 v238, v238, v177
	v_cvt_i32_f32_e32 v238, v238
	v_mul_f32_e32 v239, v239, v177
	v_cvt_i32_f32_e32 v239, v239
	ds_add_u32 v167, v224 offset:33792
	ds_add_u32 v167, v225 offset:33984
	ds_add_u32 v167, v226 offset:34176
	ds_add_u32 v167, v227 offset:34368
	ds_add_u32 v167, v228 offset:33856
	ds_add_u32 v167, v229 offset:34048
	ds_add_u32 v167, v230 offset:34240
	ds_add_u32 v167, v231 offset:34432
	ds_add_u32 v167, v232 offset:33920
	ds_add_u32 v167, v233 offset:34112
	ds_add_u32 v167, v234 offset:34304
	ds_add_u32 v167, v235 offset:34496
	s_mov_b64 exec, s[12:13]
	ds_add_u32 v168, v236 offset:49856
	s_mov_b64 exec, s[16:17]
	ds_add_u32 v168, v237 offset:49856
	s_mov_b64 exec, s[20:21]
	ds_add_u32 v168, v238 offset:49856
	s_mov_b64 exec, s[22:23]
	ds_add_u32 v168, v239 offset:49856
	s_mov_b64 exec, -1
	s_waitcnt lgkmcnt(0)
	s_barrier
	ds_read_b128 v[180:183], v170 offset:0
	ds_read_b128 v[184:187], v170 offset:1024
	ds_read_b128 v[188:191], v170 offset:2048
	ds_read_b128 v[192:195], v170 offset:3072
	ds_read_b128 v[196:199], v170 offset:4096
	ds_read_b128 v[200:203], v170 offset:5120
	ds_read_b32 v204, v171 offset:49152
	s_lshl_b32 s33, s84, 13
	s_lshl_b32 s41, s48, 8
	s_add_i32 s33, s33, s41
	s_lshl_b32 s41, s100, 5
	s_add_i32 s33, s33, s41
	s_mul_i32 s41, s33, 0xc0
	s_add_u32 s12, s26, 0x15000000
	s_addc_u32 s13, s27, 0
	s_add_u32 s12, s12, s41
	s_addc_u32 s13, s13, 0
	v_lshlrev_b32_e32 v205, 4, v164
	s_waitcnt lgkmcnt(0)
	global_store_dwordx4 v205, v[180:183], s[12:13]
	global_store_dwordx4 v205, v[184:187], s[12:13] offset:1024
	global_store_dwordx4 v205, v[188:191], s[12:13] offset:2048
	global_store_dwordx4 v205, v[192:195], s[12:13] offset:3072
	s_add_u32 s12, s12, 0x1000
	s_addc_u32 s13, s13, 0
	global_store_dwordx4 v205, v[196:199], s[12:13]
	global_store_dwordx4 v205, v[200:203], s[12:13] offset:1024
	s_lshl_b32 s41, s33, 2
	s_add_u32 s12, s26, 0x16000000
	s_addc_u32 s13, s27, 0
	s_add_u32 s12, s12, s41
	s_addc_u32 s13, s13, 0
	v_lshlrev_b32_e32 v205, 2, v164
	s_mov_b32 exec_lo, -1
	s_mov_b32 exec_hi, 0
	global_store_dword v205, v204, s[12:13]
	s_mov_b64 exec, -1
	v_mov_b64_e32 v[144:145], 0x100
	v_mov_b64_e32 v[146:147], 0xff
	s_andn2_b64 vcc, exec, s[0:1]
	s_mov_b64 s[0:1], -1
	s_cbranch_vccnz .LBB0_478
	s_andn2_b64 vcc, exec, s[4:5]
	s_cbranch_vccnz .LBB0_477
	s_barrier
	s_branch .LBB0_477

; __global__ void __launch_bounds__(512, 2) hymba_fwd(Args args) {
;     ...
;             {
;                 const bf16* xp = X1B + (size_t)(t0 + li) * DM + 256 * wave + 8 * kg;
;                 const bf16* hp = WRH + (size_t)li * DM + 256 * wave + 8 * kg; const bf16* lp = WRL + (size_t)li * DM + 256 * wave + 8 * kg;
;                 f32x4 acc[2][3]; float ss[2] = {0.f, 0.f};
; #pragma unroll
;                 for (int x = 0; x < 2; ++x)
; #pragma unroll
;                     for (int nt = 0; nt < 3; ++nt) acc[x][nt] = (f32x4){0.f, 0.f, 0.f, 0.f};
; #pragma unroll 1
;                 for (int hf = 0; hf < 2; ++hf) {
;                     v4u xa[2][4]; bf16x8 bh[4][3], bl[4][3];
; #pragma unroll
;                     for (int s4 = 0; s4 < 4; ++s4) { const int ko = 32 * (4 * hf + s4);
; #pragma unroll
;                         for (int x = 0; x < 2; ++x) xa[x][s4] = *(const v4u*)(xp + (size_t)(16 * x) * DM + ko);
; #pragma unroll
;                         for (int nt = 0; nt < 3; ++nt) { bh[s4][nt] = *(const bf16x8*)(hp + (size_t)(16 * nt) * DM + ko); bl[s4][nt] = *(const bf16x8*)(lp + (size_t)(16 * nt) * DM + ko); } }
;                     asm volatile("s_waitcnt vmcnt(0)" ::: "memory"); __builtin_amdgcn_sched_barrier(0);
; #pragma unroll
;                     for (int s4 = 0; s4 < 4; ++s4)
; #pragma unroll
;                         for (int x = 0; x < 2; ++x) { const v4u q = xa[x][s4];
;                             ss[x] += (bf_lo(q.x) * bf_lo(q.x) + bf_hi(q.x) * bf_hi(q.x)) + (bf_lo(q.y) * bf_lo(q.y) + bf_hi(q.y) * bf_hi(q.y)) + (bf_lo(q.z) * bf_lo(q.z) + bf_hi(q.z) * bf_hi(q.z)) + (bf_lo(q.w) * bf_lo(q.w) + bf_hi(q.w) * bf_hi(q.w)); }
;                     __builtin_amdgcn_sched_barrier(0);
; #pragma unroll
;                     for (int s4 = 0; s4 < 4; ++s4)
; #pragma unroll
;                         for (int x = 0; x < 2; ++x) { const bf16x8 xh = __builtin_bit_cast(bf16x8, xa[x][s4]);
; #pragma unroll
;                             for (int nt = 0; nt < 3; ++nt) {
;                                 acc[x][nt] = __builtin_amdgcn_mfma_f32_16x16x32_bf16(xh, bl[s4][nt], acc[x][nt], 0, 0, 0);
;                                 acc[x][nt] = __builtin_amdgcn_mfma_f32_16x16x32_bf16(xh, bh[s4][nt], acc[x][nt], 0, 0, 0); } }
;                 }
; #pragma unroll
;                 for (int x = 0; x < 2; ++x) {
; #pragma unroll
.LBB0_553:
	s_lshl_b32 s33, s66, 5
	s_lshl_b32 s16, s92, 13
	s_add_i32 s16, s16, s33
	s_mul_i32 s17, s16, 0xc0
	s_add_u32 s20, s26, 0x15000000
	s_addc_u32 s21, s27, 0
	s_add_u32 s20, s20, s17
	s_addc_u32 s21, s21, 0
	v_mbcnt_lo_u32_b32 v0, -1, 0
	v_mbcnt_hi_u32_b32 v0, -1, v0
	v_lshlrev_b32_e32 v1, 4, v0
	global_load_dwordx4 v[8:11], v1, s[20:21]
	global_load_dwordx4 v[12:15], v1, s[20:21] offset:1024
	global_load_dwordx4 v[16:19], v1, s[20:21] offset:2048
	global_load_dwordx4 v[20:23], v1, s[20:21] offset:3072
	s_add_u32 s20, s20, 0x1000
	s_addc_u32 s21, s21, 0
	global_load_dwordx4 v[24:27], v1, s[20:21]
	global_load_dwordx4 v[28:31], v1, s[20:21] offset:1024
	s_lshl_b32 s17, s16, 2
	s_add_u32 s20, s26, 0x16000000
	s_addc_u32 s21, s27, 0
	s_add_u32 s20, s20, s17
	s_addc_u32 s21, s21, 0
	v_lshlrev_b32_e32 v2, 2, v0
	global_load_dword v3, v2, s[20:21]
	s_mul_i32 s17, s92, 0x1800
	v_add_u32_e32 v4, s17, v1
	s_lshl_b32 s17, s92, 7
	v_add_u32_e32 v5, s17, v2
	v_mov_b32_e32 v6, 0x33800000
	v_mov_b32_e32 v7, 0x37800000
	s_waitcnt vmcnt(0)
	v_cvt_f32_i32_e32 v8, v8
	v_cvt_f32_i32_e32 v9, v9
	v_cvt_f32_i32_e32 v10, v10
	v_cvt_f32_i32_e32 v11, v11
	v_cvt_f32_i32_e32 v12, v12
	v_cvt_f32_i32_e32 v13, v13
	v_cvt_f32_i32_e32 v14, v14
	v_cvt_f32_i32_e32 v15, v15
	v_cvt_f32_i32_e32 v16, v16
	v_cvt_f32_i32_e32 v17, v17
	v_cvt_f32_i32_e32 v18, v18
	v_cvt_f32_i32_e32 v19, v19
	v_cvt_f32_i32_e32 v20, v20
	v_cvt_f32_i32_e32 v21, v21
	v_cvt_f32_i32_e32 v22, v22
	v_cvt_f32_i32_e32 v23, v23
	v_cvt_f32_i32_e32 v24, v24
	v_cvt_f32_i32_e32 v25, v25
	v_cvt_f32_i32_e32 v26, v26
	v_cvt_f32_i32_e32 v27, v27
	v_cvt_f32_i32_e32 v28, v28
	v_cvt_f32_i32_e32 v29, v29
	v_cvt_f32_i32_e32 v30, v30
	v_cvt_f32_i32_e32 v31, v31
	v_mul_f32_e32 v8, v8, v6
	v_mul_f32_e32 v9, v9, v6
	v_mul_f32_e32 v10, v10, v6
	v_mul_f32_e32 v11, v11, v6
	v_mul_f32_e32 v12, v12, v6
	v_mul_f32_e32 v13, v13, v6
	v_mul_f32_e32 v14, v14, v6
	v_mul_f32_e32 v15, v15, v6
	v_mul_f32_e32 v16, v16, v6
	v_mul_f32_e32 v17, v17, v6
	v_mul_f32_e32 v18, v18, v6
	v_mul_f32_e32 v19, v19, v6
	v_mul_f32_e32 v20, v20, v6
	v_mul_f32_e32 v21, v21, v6
	v_mul_f32_e32 v22, v22, v6
	v_mul_f32_e32 v23, v23, v6
	v_mul_f32_e32 v24, v24, v6
	v_mul_f32_e32 v25, v25, v6
	v_mul_f32_e32 v26, v26, v6
	v_mul_f32_e32 v27, v27, v6
	v_mul_f32_e32 v28, v28, v6
	v_mul_f32_e32 v29, v29, v6
	v_mul_f32_e32 v30, v30, v6
	v_mul_f32_e32 v31, v31, v6
	v_cvt_f32_i32_e32 v3, v3
	s_nop 0
	v_mul_f32_e32 v3, v3, v7
	ds_write_b128 v4, v[8:11]
	ds_write_b128 v4, v[12:15] offset:1024
	ds_write_b128 v4, v[16:19] offset:2048
	ds_write_b128 v4, v[20:23] offset:3072
	ds_write_b128 v4, v[24:27] offset:4096
	ds_write_b128 v4, v[28:31] offset:5120
	s_mov_b32 exec_lo, -1
	s_mov_b32 exec_hi, 0
	ds_write_b32 v5, v3 offset:55296
	s_mov_b64 exec, -1
	s_waitcnt lgkmcnt(0)
	s_barrier
	s_and_saveexec_b64 s[12:13], s[14:15]
	s_cbranch_execz .LBB0_572
	s_mov_b64 s[20:21], -1
	v_mov_b32_e32 v1, v152
	s_and_saveexec_b64 s[16:17], s[18:19]
	s_cbranch_execz .LBB0_569
	v_mov_b32_e32 v2, 0
	s_and_saveexec_b64 s[20:21], s[6:7]
	s_cbranch_execz .LBB0_565
	s_mov_b32 s42, 0
	s_mov_b64 s[46:47], 0
	v_mov_b32_e32 v0, v179
	v_mov_b32_e32 v1, v176
